# stack7 + attention unit epilogues read all 1/l normalisers from LDS at once (one wait) instead of 16 serialized LDS round trips per unit
# baseline (speedup 1.0000x reference)
; #define LAS __attribute__((address_space(3)))
; __device__ __forceinline__ float shx(float v, int m, int lane) { return __int_as_float(__builtin_amdgcn_ds_bpermute((lane ^ m) << 2, __float_as_int(v))); }
; __device__ __forceinline__ int crow(int r, int hi) { return (r & 3) + 8 * (r >> 2) + 4 * hi; }
; __device__ __forceinline__ void unit_diff(const P& p, LAS unsigned char* lds, const Src& S, float lam, bf16_t* orow, const int wid,
;                                           bf16x8 (&qr)[4], const bool pre  , const bool pn  , const Src& Sn) {
;     ...
;     l1 += shx(l1, 32, lane); l2 += shx(l2, 32, lane);
;     LAS float* wsf = (LAS float*)(lds + WS_OFF + wid * 256);
;     if (hi == 0) { wsf[r32] = 1.0f / l1; wsf[32 + r32] = lam / l2; }
;     asm volatile("s_waitcnt lgkmcnt(0)" ::: "memory");
;     LAS float* stg = (LAS float*)(lds + 2 * SLOTB + wid * STG_W);
; #pragma unroll
;     for (int r = 0; r < 16; ++r) { const int qrow = crow(r, hi); const float i1 = wsf[qrow], i2 = wsf[32 + qrow];
; #pragma unroll
;         for (int d0 = 0; d0 < 2; ++d0) stg[qrow * 68 + d0 * 32 + r32] = o1[d0][r] * i1 - o2[d0][r] * i2; }
;     asm volatile("s_waitcnt lgkmcnt(0)" ::: "memory");
.LBB7_443:
	s_or_b64 exec, exec, s[58:59]
	s_waitcnt lgkmcnt(0)
	v_lshl_add_u32 v65, v170, 4, s97
	s_waitcnt lgkmcnt(0)
	ds_read_b32 v213, v65 offset:128
	ds_read_b32 v214, v65
	ds_read_b32 v215, v65 offset:132
	ds_read_b32 v216, v65 offset:4
	ds_read_b32 v217, v65 offset:136
	ds_read_b32 v218, v65 offset:8
	ds_read_b32 v219, v65 offset:140
	ds_read_b32 v220, v65 offset:12
	ds_read_b32 v221, v65 offset:160
	ds_read_b32 v222, v65 offset:32
	ds_read_b32 v223, v65 offset:164
	ds_read_b32 v224, v65 offset:36
	ds_read_b32 v225, v65 offset:168
	ds_read_b32 v226, v65 offset:40
	ds_read_b32 v227, v65 offset:172
	ds_read_b32 v228, v65 offset:44
	ds_read_b32 v229, v65 offset:192
	ds_read_b32 v230, v65 offset:64
	ds_read_b32 v231, v65 offset:196
	ds_read_b32 v232, v65 offset:68
	ds_read_b32 v233, v65 offset:200
	ds_read_b32 v234, v65 offset:72
	ds_read_b32 v235, v65 offset:204
	ds_read_b32 v236, v65 offset:76
	ds_read_b32 v237, v65 offset:224
	ds_read_b32 v238, v65 offset:96
	ds_read_b32 v239, v65 offset:228
	ds_read_b32 v240, v65 offset:100
	ds_read_b32 v241, v65 offset:232
	ds_read_b32 v242, v65 offset:104
	ds_read_b32 v243, v65 offset:236
	ds_read_b32 v244, v65 offset:108
	s_waitcnt lgkmcnt(0)
	v_mov_b32_e32 v67, v213
	v_mov_b32_e32 v70, v214
	v_lshl_add_u32 v66, v171, 2, s93
	s_movk_i32 s10, 0x440
	v_mul_f32_e32 v32, v32, v67
	v_mad_u64_u32 v[68:69], s[10:11], v170, s10, v[66:67]
	v_fma_f32 v0, v0, v70, -v32
	v_mul_f32_e32 v32, v48, v67
	v_fma_f32 v16, v16, v70, -v32
	v_add_u32_e32 v32, 0x8000, v68
	ds_write2_b32 v32, v0, v16 offset1:32
	v_mov_b32_e32 v0, v215
	v_mov_b32_e32 v16, v216
	v_lshl_or_b32 v32, v170, 2, 1
	v_mad_u64_u32 v[66:67], s[10:11], v32, s40, v[66:67]
	v_mul_f32_e32 v32, v33, v0
	v_mul_f32_e32 v0, v49, v0
	v_fma_f32 v1, v1, v16, -v32
	v_fma_f32 v0, v17, v16, -v0
	v_add_u32_e32 v16, 0x8000, v66
	ds_write2_b32 v16, v1, v0 offset1:32
	v_mov_b32_e32 v0, v217
	v_mov_b32_e32 v1, v218
	v_ashrrev_i32_e32 v32, 1, v169
	s_ashr_i32 s10, s95, 7
	s_ashr_i32 s11, s10, 31
	v_mul_f32_e32 v17, v34, v0
	v_mul_f32_e32 v0, v50, v0
	v_fma_f32 v2, v2, v1, -v17
	v_fma_f32 v0, v18, v1, -v0
	ds_write2_b32 v16, v2, v0 offset0:68 offset1:100
	v_mov_b32_e32 v0, v219
	v_mov_b32_e32 v1, v220
	s_lshl_b64 s[58:59], s[10:11], 23
	v_readlane_b32 s10, v254, 43
	s_add_u32 s13, s10, s58
	v_mul_f32_e32 v2, v35, v0
	v_mul_f32_e32 v0, v51, v0
	v_fma_f32 v2, v3, v1, -v2
	v_fma_f32 v0, v19, v1, -v0
	ds_write2_b32 v16, v2, v0 offset0:136 offset1:168
	v_mov_b32_e32 v0, v221
	v_mov_b32_e32 v1, v222
	v_readlane_b32 s10, v254, 42
	s_addc_u32 s36, s10, s59
	s_lshl_b64 s[10:11], s[8:9], 11
	v_mul_f32_e32 v2, v36, v0
	v_mul_f32_e32 v0, v52, v0
	v_fma_f32 v2, v4, v1, -v2
	v_fma_f32 v0, v20, v1, -v0
	v_add_u32_e32 v1, 0x8400, v66
	ds_write2_b32 v1, v2, v0 offset0:220 offset1:252
	v_mov_b32_e32 v0, v223
	v_mov_b32_e32 v1, v224
	s_add_u32 s8, s13, s10
	s_mov_b32 s10, 0x800000
	s_addc_u32 s11, s36, s11
	v_mul_f32_e32 v2, v37, v0
	v_mul_f32_e32 v0, v53, v0
	v_fma_f32 v2, v5, v1, -v2
	v_fma_f32 v0, v21, v1, -v0
	v_add_u32_e32 v1, 0x8800, v66
	ds_write2_b32 v1, v2, v0 offset0:32 offset1:64
	v_mov_b32_e32 v0, v225
	v_mov_b32_e32 v2, v226
	s_lshl_b32 s2, s2, 7
	s_mov_b64 s[58:59], -1
	v_mul_f32_e32 v3, v38, v0
	v_mul_f32_e32 v0, v54, v0
	v_fma_f32 v3, v6, v2, -v3
	v_fma_f32 v0, v22, v2, -v0
	ds_write2_b32 v1, v3, v0 offset0:100 offset1:132
	v_mov_b32_e32 v0, v227
	v_mov_b32_e32 v2, v228
	v_mul_f32_e32 v3, v39, v0
	v_mul_f32_e32 v0, v55, v0
	v_fma_f32 v3, v7, v2, -v3
	v_fma_f32 v0, v23, v2, -v0
	ds_write2_b32 v1, v3, v0 offset0:168 offset1:200
	v_mov_b32_e32 v0, v229
	v_mov_b32_e32 v1, v230
	v_mul_f32_e32 v2, v40, v0
	v_mul_f32_e32 v0, v56, v0
	v_fma_f32 v2, v8, v1, -v2
	v_fma_f32 v0, v24, v1, -v0
	v_add_u32_e32 v1, 0x8e00, v66
	ds_write2_b32 v1, v2, v0 offset0:124 offset1:156
	v_mov_b32_e32 v0, v231
	v_mov_b32_e32 v1, v232
	v_mul_f32_e32 v2, v41, v0
	v_mul_f32_e32 v0, v57, v0
	v_fma_f32 v2, v9, v1, -v2
	v_fma_f32 v0, v25, v1, -v0
	v_add_u32_e32 v1, 0x9000, v66
	ds_write2_b32 v1, v2, v0 offset0:64 offset1:96
	v_mov_b32_e32 v0, v233
	v_mov_b32_e32 v2, v234
	v_mul_f32_e32 v3, v42, v0
	v_mul_f32_e32 v0, v58, v0
	v_fma_f32 v3, v10, v2, -v3
	v_fma_f32 v0, v26, v2, -v0
	ds_write2_b32 v1, v3, v0 offset0:132 offset1:164
	v_mov_b32_e32 v0, v235
	v_mov_b32_e32 v2, v236
	v_mul_f32_e32 v3, v43, v0
	v_mul_f32_e32 v0, v59, v0
	v_fma_f32 v3, v11, v2, -v3
	v_fma_f32 v0, v27, v2, -v0
	ds_write2_b32 v1, v3, v0 offset0:200 offset1:232
	v_mov_b32_e32 v0, v237
	v_mov_b32_e32 v1, v238
	v_mul_f32_e32 v2, v44, v0
	v_mul_f32_e32 v0, v60, v0
	v_fma_f32 v2, v12, v1, -v2
	v_fma_f32 v0, v28, v1, -v0
	v_add_u32_e32 v1, 0x9800, v66
	ds_write2_b32 v1, v2, v0 offset0:28 offset1:60
	v_mov_b32_e32 v0, v239
	v_mov_b32_e32 v2, v240
	v_mul_f32_e32 v3, v45, v0
	v_mul_f32_e32 v0, v61, v0
	v_fma_f32 v3, v13, v2, -v3
	v_fma_f32 v0, v29, v2, -v0
	ds_write2_b32 v1, v3, v0 offset0:96 offset1:128
	v_mov_b32_e32 v0, v241
	v_mov_b32_e32 v2, v242
	v_mul_f32_e32 v3, v46, v0
	v_mul_f32_e32 v0, v62, v0
	v_fma_f32 v3, v14, v2, -v3
	v_fma_f32 v0, v30, v2, -v0
	ds_write2_b32 v1, v3, v0 offset0:164 offset1:196
	v_mov_b32_e32 v0, v243
	v_mov_b32_e32 v1, v244
	v_mul_f32_e32 v2, v47, v0
	v_mul_f32_e32 v0, v63, v0
	v_fma_f32 v2, v15, v1, -v2
	v_fma_f32 v0, v31, v1, -v0
	v_add_u32_e32 v1, 0x9a00, v66
	ds_write2_b32 v1, v2, v0 offset0:104 offset1:136
	v_lshlrev_b32_e32 v1, 5, v169
	v_and_b32_e32 v42, 32, v1
	v_mul_lo_u32 v0, v32, s40
	v_lshlrev_b32_e32 v43, 2, v42
	s_waitcnt lgkmcnt(0)
	v_add3_u32 v30, s93, v0, v43
	ds_read_b128 v[0:3], v30 offset:32768
	ds_read_b128 v[4:7], v30 offset:32784
	ds_read_b128 v[8:11], v30 offset:32800
	ds_read_b128 v[12:15], v30 offset:32816
	v_lshlrev_b32_e32 v156, 1, v42
	s_waitcnt lgkmcnt(0)
; #define LAS __attribute__((address_space(3)))
; __device__ __forceinline__ float shx(float v, int m, int lane) { return __int_as_float(__builtin_amdgcn_ds_bpermute((lane ^ m) << 2, __float_as_int(v))); }
; __device__ __forceinline__ unsigned cvtpk(float lo, float hi) { unsigned r; asm volatile("v_cvt_pk_bf16_f32 %0, %1, %2" : "=v"(r) : "v"(lo), "v"(hi)); return r; }
; #define ATT_BAR() do { asm volatile("s_waitcnt lgkmcnt(0)" ::: "memory"); __builtin_amdgcn_s_barrier(); asm volatile("" ::: "memory"); } while (0)
; __device__ __forceinline__ void unit_diff(const P& p, LAS unsigned char* lds, const Src& S, float lam, bf16_t* orow, const int wid,
;                                           bf16x8 (&qr)[4], const bool pre  , const bool pn  , const Src& Sn) {
;     ...
;     { const int row = lane >> 1, hf = lane & 1; const LAS f32x4* src = (const LAS f32x4*)(stg + row * 68 + hf * 32); f32x4 v[8]; float ss = 0.f;
; #pragma unroll
;       for (int i = 0; i < 8; ++i) { v[i] = src[i]; ss += (v[i][0] * v[i][0] + v[i][1] * v[i][1]) + (v[i][2] * v[i][2] + v[i][3] * v[i][3]); }
;       ss += shx(ss, 1, lane); const float sc = rsqrtf(ss * (1.0f / 64.0f) + 1e-5f) * 0.8f;
;       bf16_t* dst = orow + (size_t)row * DM + hf * 32;
;       const LAS float* gdh = (const LAS float*)(lds + GDH_OFF);
; #pragma unroll
;       for (int i = 0; i < 4; ++i) { const f32x4 a = v[2 * i] * sc * *(const LAS f32x4*)(gdh + hf * 32 + 8 * i), c = v[2 * i + 1] * sc * *(const LAS f32x4*)(gdh + hf * 32 + 8 * i + 4);
;           u32x4 w; w.x = cvtpk(a[0], a[1]); w.y = cvtpk(a[2], a[3]); w.z = cvtpk(c[0], c[1]); w.w = cvtpk(c[2], c[3]); *(u32x4*)(dst + 8 * i) = w; } }
;     if (pn) {
; #pragma unroll
;         for (int d0 = 0; d0 < 4; ++d0) qr[d0] = qn[d0]; }
;     else ATT_BAR();
	v_mov_b32_e32 v18, v1
	v_mov_b32_e32 v19, v5
	v_mov_b32_e32 v16, v0
	v_mov_b32_e32 v17, v4
	v_pk_mul_f32 v[18:19], v[18:19], v[18:19]
	v_mov_b32_e32 v20, v3
	v_mov_b32_e32 v21, v7
	v_pk_fma_f32 v[16:17], v[16:17], v[16:17], v[18:19]
	v_mov_b32_e32 v18, v2
	v_mov_b32_e32 v19, v6
	v_pk_mul_f32 v[20:21], v[20:21], v[20:21]
	v_pk_mul_f32 v[22:23], v[8:9], v[8:9]
	v_pk_fma_f32 v[18:19], v[18:19], v[18:19], v[20:21]
	v_pk_mul_f32 v[20:21], v[10:11], v[10:11]
	v_pk_add_f32 v[24:25], v[16:17], v[18:19]
	ds_read_b128 v[16:19], v30 offset:32832
	v_pk_mov_b32 v[26:27], v[22:23], v[20:21] op_sel:[1,0]
	v_mov_b32_e32 v23, v21
	v_pk_add_f32 v[26:27], v[26:27], v[22:23]
	ds_read_b128 v[20:23], v30 offset:32848
	s_waitcnt lgkmcnt(0)
	v_mul_f32_e32 v28, v16, v16
	v_mul_f32_e32 v29, v17, v17
	v_pk_add_f32 v[24:25], v[24:25], v[24:25] op_sel:[0,1] op_sel_hi:[1,0]
	v_pk_add_f32 v[26:27], v[26:27], v[26:27] op_sel:[0,1] op_sel_hi:[1,0]
	v_mov_b32_e32 v25, v28
	v_mov_b32_e32 v27, v29
	v_pk_add_f32 v[24:25], v[24:25], v[26:27]
	v_mul_f32_e32 v26, v13, v13
	v_mul_f32_e32 v28, v15, v15
	v_mul_f32_e32 v31, v18, v18
	v_mul_f32_e32 v33, v19, v19
	v_pk_fma_f32 v[26:27], v[12:13], v[12:13], v[26:27] op_sel_hi:[1,1,0]
	v_pk_fma_f32 v[28:29], v[14:15], v[14:15], v[28:29] op_sel_hi:[1,1,0]
	v_mov_b32_e32 v27, v31
	v_mov_b32_e32 v29, v33
	v_pk_add_f32 v[26:27], v[26:27], v[28:29]
	v_pk_mul_f32 v[36:37], v[22:23], v[22:23]
	v_pk_add_f32 v[34:35], v[24:25], v[26:27]
	ds_read_b128 v[24:27], v30 offset:32864
	ds_read_b128 v[28:31], v30 offset:32880
	v_pk_mul_f32 v[38:39], v[20:21], v[20:21]
	v_pk_add_f32 v[34:35], v[34:35], v[34:35] op_sel:[0,1] op_sel_hi:[1,0]
	v_pk_mov_b32 v[40:41], v[38:39], v[36:37] op_sel:[1,0]
	v_mov_b32_e32 v39, v37
	v_pk_add_f32 v[36:37], v[40:41], v[38:39]
	s_waitcnt lgkmcnt(0)
	v_mul_f32_e32 v33, v28, v28
	v_mul_f32_e32 v38, v29, v29
	v_pk_add_f32 v[36:37], v[36:37], v[36:37] op_sel:[0,1] op_sel_hi:[1,0]
	v_mov_b32_e32 v35, v33
	v_mov_b32_e32 v37, v38
	v_pk_add_f32 v[34:35], v[34:35], v[36:37]
	v_mul_f32_e32 v36, v25, v25
	v_mul_f32_e32 v39, v30, v30
	v_pk_fma_f32 v[36:37], v[24:25], v[24:25], v[36:37] op_sel_hi:[1,1,0]
	v_mul_f32_e32 v38, v27, v27
	v_mul_f32_e32 v40, v31, v31
	v_mov_b32_e32 v37, v39
	v_pk_fma_f32 v[38:39], v[26:27], v[26:27], v[38:39] op_sel_hi:[1,1,0]
	s_nop 0
	v_mov_b32_e32 v39, v40
	v_pk_add_f32 v[36:37], v[36:37], v[38:39]
	s_nop 0
	v_pk_add_f32 v[34:35], v[34:35], v[36:37]
	s_nop 0
	v_add_f32_e32 v33, v34, v35
	v_xor_b32_e32 v34, 4, v64
	ds_bpermute_b32 v34, v34, v33
	s_waitcnt lgkmcnt(0)
	v_add_f32_e32 v33, v33, v34
	v_fmamk_f32 v33, v33, 0x3c800000, v167
	v_mul_f32_e32 v34, 0x4b800000, v33
	v_cmp_gt_f32_e32 vcc, s10, v33
	s_add_u32 s10, s8, s2
	s_addc_u32 s11, s11, 0
	v_cndmask_b32_e32 v33, v33, v34, vcc
	v_rsq_f32_e32 v33, v33
	s_nop 0
	v_mul_f32_e32 v34, 0x45800000, v33
	v_cndmask_b32_e32 v33, v33, v34, vcc
	v_mul_f32_e32 v36, 0x3f4ccccd, v33
	v_ashrrev_i32_e32 v33, 31, v32
	v_lshlrev_b64 v[32:33], 11, v[32:33]
	v_lshl_add_u64 v[38:39], s[10:11], 0, v[32:33]
	v_add_u32_e32 v32, 0, v43
	v_add_u32_e32 v37, 0x1d800, v32
	ds_read_b128 v[32:35], v37
	v_pk_mul_f32 v[40:41], v[0:1], v[36:37] op_sel_hi:[1,0]
	v_pk_mul_f32 v[42:43], v[2:3], v[36:37] op_sel_hi:[1,0]
	ds_read_b128 v[0:3], v37 offset:16
	v_pk_mul_f32 v[4:5], v[4:5], v[36:37] op_sel_hi:[1,0]
	v_pk_mul_f32 v[6:7], v[6:7], v[36:37] op_sel_hi:[1,0]
	v_lshl_add_u64 v[38:39], v[38:39], 0, v[156:157]
	s_waitcnt lgkmcnt(0)
	v_pk_mul_f32 v[34:35], v[34:35], v[42:43]
	v_pk_mul_f32 v[6:7], v[2:3], v[6:7]
	v_pk_mul_f32 v[2:3], v[0:1], v[4:5]
	v_pk_mul_f32 v[32:33], v[32:33], v[40:41]
	v_pk_mul_f32 v[8:9], v[8:9], v[36:37] op_sel_hi:[1,0]
	v_cvt_pk_bf16_f32 v0, v32, v33
	v_cvt_pk_bf16_f32 v1, v34, v35
	v_cvt_pk_bf16_f32 v2, v2, v3
	v_cvt_pk_bf16_f32 v3, v6, v7
	ds_read_b128 v[4:7], v37 offset:32
	global_store_dwordx4 v[38:39], v[0:3], off offset:1024
	ds_read_b128 v[0:3], v37 offset:48
	v_pk_mul_f32 v[10:11], v[10:11], v[36:37] op_sel_hi:[1,0]
	s_and_b64 vcc, exec, s[56:57]
	s_waitcnt lgkmcnt(0)
	v_pk_mul_f32 v[6:7], v[6:7], v[10:11]
	v_pk_mul_f32 v[4:5], v[4:5], v[8:9]
	v_pk_mul_f32 v[8:9], v[12:13], v[36:37] op_sel_hi:[1,0]
	v_pk_mul_f32 v[10:11], v[14:15], v[36:37] op_sel_hi:[1,0]
	s_nop 0
	v_pk_mul_f32 v[10:11], v[2:3], v[10:11]
	v_pk_mul_f32 v[2:3], v[0:1], v[8:9]
	v_cvt_pk_bf16_f32 v0, v4, v5
	v_cvt_pk_bf16_f32 v1, v6, v7
	v_pk_mul_f32 v[8:9], v[16:17], v[36:37] op_sel_hi:[1,0]
	v_cvt_pk_bf16_f32 v2, v2, v3
	v_cvt_pk_bf16_f32 v3, v10, v11
	ds_read_b128 v[4:7], v37 offset:64
	global_store_dwordx4 v[38:39], v[0:3], off offset:1040
	ds_read_b128 v[0:3], v37 offset:80
	v_pk_mul_f32 v[10:11], v[18:19], v[36:37] op_sel_hi:[1,0]
	s_waitcnt lgkmcnt(0)
	v_pk_mul_f32 v[4:5], v[4:5], v[8:9]
	v_pk_mul_f32 v[6:7], v[6:7], v[10:11]
	v_pk_mul_f32 v[8:9], v[20:21], v[36:37] op_sel_hi:[1,0]
	v_pk_mul_f32 v[10:11], v[22:23], v[36:37] op_sel_hi:[1,0]
	s_nop 0
	v_pk_mul_f32 v[10:11], v[10:11], v[2:3]
	v_pk_mul_f32 v[2:3], v[8:9], v[0:1]
	v_cvt_pk_bf16_f32 v0, v4, v5
	v_cvt_pk_bf16_f32 v1, v6, v7
	v_pk_mul_f32 v[8:9], v[24:25], v[36:37] op_sel_hi:[1,0]
	v_cvt_pk_bf16_f32 v2, v2, v3
	v_cvt_pk_bf16_f32 v3, v10, v11
	ds_read_b128 v[4:7], v37 offset:96
	global_store_dwordx4 v[38:39], v[0:3], off offset:1056
	ds_read_b128 v[0:3], v37 offset:112
	v_pk_mul_f32 v[10:11], v[26:27], v[36:37] op_sel_hi:[1,0]
	s_waitcnt lgkmcnt(0)
	v_pk_mul_f32 v[4:5], v[8:9], v[4:5]
	v_pk_mul_f32 v[6:7], v[10:11], v[6:7]
	v_pk_mul_f32 v[8:9], v[28:29], v[36:37] op_sel_hi:[1,0]
	v_pk_mul_f32 v[10:11], v[30:31], v[36:37] op_sel_hi:[1,0]
	s_nop 0
	v_pk_mul_f32 v[10:11], v[10:11], v[2:3]
	v_pk_mul_f32 v[2:3], v[8:9], v[0:1]
	v_cvt_pk_bf16_f32 v0, v4, v5
	v_cvt_pk_bf16_f32 v1, v6, v7
	s_nop 0
	v_cvt_pk_bf16_f32 v2, v2, v3
	v_cvt_pk_bf16_f32 v3, v10, v11
	global_store_dwordx4 v[38:39], v[0:3], off offset:1072
	s_cbranch_vccz .LBB7_396
	s_waitcnt lgkmcnt(0)
	s_barrier
	v_mov_b32_e32 v145, v143
	v_mov_b32_e32 v150, v142
	v_mov_b32_e32 v151, v141
	v_mov_b32_e32 v152, v140
	v_mov_b32_e32 v153, v139
	v_mov_b32_e32 v154, v138
	v_mov_b32_e32 v155, v137
	v_mov_b32_e32 v160, v136
	v_mov_b32_e32 v161, v135
	v_mov_b32_e32 v172, v134
	v_mov_b32_e32 v173, v133
	v_mov_b32_e32 v174, v132
	v_mov_b32_e32 v175, v131
	v_mov_b32_e32 v176, v130
	v_mov_b32_e32 v177, v129
	v_mov_b32_e32 v178, v128
	s_cbranch_execz .LBB7_397

; #define LAS __attribute__((address_space(3)))
; __device__ __forceinline__ float shx(float v, int m, int lane) { return __int_as_float(__builtin_amdgcn_ds_bpermute((lane ^ m) << 2, __float_as_int(v))); }
; __device__ __forceinline__ int crow(int r, int hi) { return (r & 3) + 8 * (r >> 2) + 4 * hi; }
; __device__ __forceinline__ unsigned cvtpk(float lo, float hi) { unsigned r; asm volatile("v_cvt_pk_bf16_f32 %0, %1, %2" : "=v"(r) : "v"(lo), "v"(hi)); return r; }
; #define ATT_BAR() do { asm volatile("s_waitcnt lgkmcnt(0)" ::: "memory"); __builtin_amdgcn_s_barrier(); asm volatile("" ::: "memory"); } while (0)
; __device__ __forceinline__ void unit_swa(const P& p, LAS unsigned char* lds, const Src& S, const int qa  , const float sinkp, bf16_t* orow, const int wid,
;                                          bf16x8 (&qr)[4], const bool pre, const bool pn, const Src& Sn) {
;     ...
;     l1 += shx(l1, 32, lane); l1 += sinkp;
;     LAS float* wsf = (LAS float*)(lds + WS_OFF + wid * 256);
;     if (hi == 0) wsf[r32] = 1.0f / l1;
;     asm volatile("s_waitcnt lgkmcnt(0)" ::: "memory");
;     LAS float* stg = (LAS float*)(lds + 2 * SLOTB + wid * STG_W);
; #pragma unroll
;     for (int r = 0; r < 16; ++r) { const int qrow = crow(r, hi); const float i1 = wsf[qrow];
; #pragma unroll
;         for (int d0 = 0; d0 < 2; ++d0) stg[qrow * 68 + d0 * 32 + r32] = o1[d0][r] * i1; }
;     asm volatile("s_waitcnt lgkmcnt(0)" ::: "memory");
;     { const int row = lane >> 1, hf = lane & 1; const LAS f32x4* src = (const LAS f32x4*)(stg + row * 68 + hf * 32); bf16_t* dst = orow + (size_t)row * DM + hf * 32;
; #pragma unroll
;       for (int i = 0; i < 4; ++i) { const f32x4 a = src[2 * i], c = src[2 * i + 1];
;           u32x4 w; w.x = cvtpk(a[0], a[1]); w.y = cvtpk(a[2], a[3]); w.z = cvtpk(c[0], c[1]); w.w = cvtpk(c[2], c[3]); *(u32x4*)(dst + 8 * i) = w; } }
;     if (pn) {
; #pragma unroll
;         for (int d0 = 0; d0 < 4; ++d0) qr[d0] = qn[d0]; }
;     else ATT_BAR();
.LBB7_512:
	s_or_b64 exec, exec, s[50:51]
	s_waitcnt lgkmcnt(0)
	v_lshl_add_u32 v52, v112, 2, s52
	s_waitcnt lgkmcnt(0)
	ds_read_b32 v213, v52
	ds_read_b32 v214, v52 offset:4
	ds_read_b32 v215, v52 offset:8
	ds_read_b32 v216, v52 offset:12
	ds_read_b32 v217, v52 offset:32
	ds_read_b32 v218, v52 offset:36
	ds_read_b32 v219, v52 offset:40
	ds_read_b32 v220, v52 offset:44
	ds_read_b32 v221, v52 offset:64
	ds_read_b32 v222, v52 offset:68
	ds_read_b32 v223, v52 offset:72
	ds_read_b32 v224, v52 offset:76
	ds_read_b32 v225, v52 offset:96
	ds_read_b32 v226, v52 offset:100
	ds_read_b32 v227, v52 offset:104
	ds_read_b32 v228, v52 offset:108
	s_waitcnt lgkmcnt(0)
	v_mov_b32_e32 v49, v213
	v_lshl_add_u32 v48, v110, 2, s53
	s_movk_i32 s1, 0x440
	s_xor_b64 s[48:49], s[48:49], -1
	v_readlane_b32 s6, v254, 43
	v_mad_u64_u32 v[50:51], s[36:37], v109, s1, v[48:49]
	v_mul_f32_e32 v0, v0, v49
	v_mul_f32_e32 v16, v16, v49
	v_add_u32_e32 v49, 0x8000, v50
	ds_write2_b32 v49, v0, v16 offset1:32
	v_mov_b32_e32 v0, v214
	v_or_b32_e32 v16, 1, v112
	v_mad_u64_u32 v[48:49], s[36:37], v16, s40, v[48:49]
	v_add_u32_e32 v16, 0x8000, v48
	v_mul_f32_e32 v1, v1, v0
	v_mul_f32_e32 v0, v17, v0
	ds_write2_b32 v16, v1, v0 offset1:32
	v_mov_b32_e32 v0, v215
	s_ashr_i32 s1, s0, 31
	s_lshl_b64 s[0:1], s[0:1], 23
	s_add_u32 s0, s6, s0
	v_readlane_b32 s6, v254, 42
	v_mul_f32_e32 v1, v2, v0
	v_mul_f32_e32 v0, v18, v0
	ds_write2_b32 v16, v1, v0 offset0:68 offset1:100
	v_mov_b32_e32 v0, v216
	s_addc_u32 s1, s6, s1
	s_lshl_b32 s6, s9, 11
	s_add_u32 s0, s0, s6
	s_addc_u32 s1, s1, 0
	v_mul_f32_e32 v1, v3, v0
	v_mul_f32_e32 v0, v19, v0
	ds_write2_b32 v16, v1, v0 offset0:136 offset1:168
	v_mov_b32_e32 v0, v217
	v_add_u32_e32 v1, 0x8400, v48
	s_lshl_b32 s6, s8, 7
	s_add_u32 s0, s0, s6
	s_addc_u32 s1, s1, 0
	v_mul_f32_e32 v2, v4, v0
	v_mul_f32_e32 v0, v20, v0
	ds_write2_b32 v1, v2, v0 offset0:220 offset1:252
	v_mov_b32_e32 v0, v218
	v_add_u32_e32 v1, 0x8800, v48
	v_add_u32_e32 v4, 0x9800, v48
	s_and_b64 vcc, exec, s[48:49]
	v_mul_f32_e32 v2, v5, v0
	v_mul_f32_e32 v0, v21, v0
	ds_write2_b32 v1, v2, v0 offset0:32 offset1:64
	v_mov_b32_e32 v0, v219
	v_mul_f32_e32 v2, v6, v0
	v_mul_f32_e32 v0, v22, v0
	ds_write2_b32 v1, v2, v0 offset0:100 offset1:132
	v_mov_b32_e32 v0, v220
	v_add_u32_e32 v6, 0x9a00, v48
	v_mul_f32_e32 v2, v7, v0
	v_mul_f32_e32 v0, v23, v0
	ds_write2_b32 v1, v2, v0 offset0:168 offset1:200
	v_mov_b32_e32 v0, v221
	v_add_u32_e32 v1, 0x8e00, v48
	v_mul_f32_e32 v2, v8, v0
	v_mul_f32_e32 v0, v24, v0
	ds_write2_b32 v1, v2, v0 offset0:124 offset1:156
	v_mov_b32_e32 v0, v222
	v_add_u32_e32 v1, 0x9000, v48
	v_mul_f32_e32 v2, v9, v0
	v_mul_f32_e32 v0, v25, v0
	ds_write2_b32 v1, v2, v0 offset0:64 offset1:96
	v_mov_b32_e32 v0, v223
	v_mul_f32_e32 v2, v10, v0
	v_mul_f32_e32 v0, v26, v0
	ds_write2_b32 v1, v2, v0 offset0:132 offset1:164
	v_mov_b32_e32 v2, v224
	v_ashrrev_i32_e32 v0, 1, v108
	v_mul_f32_e32 v3, v11, v2
	v_mul_f32_e32 v2, v27, v2
	ds_write2_b32 v1, v3, v2 offset0:200 offset1:232
	v_mov_b32_e32 v1, v225
	v_mul_lo_u32 v3, v0, s40
	v_lshlrev_b32_e32 v2, 5, v108
	v_and_b32_e32 v2, 32, v2
	v_lshlrev_b32_e32 v144, 1, v2
	v_mul_f32_e32 v5, v12, v1
	v_mul_f32_e32 v1, v28, v1
	ds_write2_b32 v4, v5, v1 offset0:28 offset1:60
	v_mov_b32_e32 v5, v226
	v_ashrrev_i32_e32 v1, 31, v0
	v_lshlrev_b64 v[8:9], 11, v[0:1]
	v_mul_f32_e32 v7, v13, v5
	v_mul_f32_e32 v5, v29, v5
	ds_write2_b32 v4, v7, v5 offset0:96 offset1:128
	v_mov_b32_e32 v5, v227
	v_lshlrev_b32_e32 v7, 2, v2
	v_lshl_add_u64 v[12:13], s[0:1], 0, v[8:9]
	v_lshl_add_u64 v[12:13], v[12:13], 0, v[144:145]
	s_mov_b64 s[0:1], -1
	v_mul_f32_e32 v0, v14, v5
	v_mul_f32_e32 v1, v30, v5
	ds_write2_b32 v4, v0, v1 offset0:164 offset1:196
	v_mov_b32_e32 v0, v228
	v_add3_u32 v14, s53, v3, v7
	v_mul_f32_e32 v1, v15, v0
	v_mul_f32_e32 v0, v31, v0
	ds_write2_b32 v6, v1, v0 offset0:104 offset1:136
	s_waitcnt lgkmcnt(0)
	ds_read_b128 v[0:3], v14 offset:32768
	ds_read_b128 v[4:7], v14 offset:32784
	s_waitcnt lgkmcnt(0)
	v_cvt_pk_bf16_f32 v0, v0, v1
	v_cvt_pk_bf16_f32 v1, v2, v3
	v_cvt_pk_bf16_f32 v2, v4, v5
	v_cvt_pk_bf16_f32 v3, v6, v7
	ds_read_b128 v[4:7], v14 offset:32800
	ds_read_b128 v[8:11], v14 offset:32816
	global_store_dwordx4 v[12:13], v[0:3], off
	s_waitcnt lgkmcnt(0)
	s_nop 0
	v_cvt_pk_bf16_f32 v0, v4, v5
	v_cvt_pk_bf16_f32 v1, v6, v7
	v_cvt_pk_bf16_f32 v2, v8, v9
	v_cvt_pk_bf16_f32 v3, v10, v11
	ds_read_b128 v[4:7], v14 offset:32832
	ds_read_b128 v[8:11], v14 offset:32848
	global_store_dwordx4 v[12:13], v[0:3], off offset:16
	s_waitcnt lgkmcnt(0)
	s_nop 0
	v_cvt_pk_bf16_f32 v0, v4, v5
	v_cvt_pk_bf16_f32 v1, v6, v7
	v_cvt_pk_bf16_f32 v2, v8, v9
	v_cvt_pk_bf16_f32 v3, v10, v11
	ds_read_b128 v[4:7], v14 offset:32864
	ds_read_b128 v[8:11], v14 offset:32880
	global_store_dwordx4 v[12:13], v[0:3], off offset:32
	s_waitcnt lgkmcnt(0)
	s_nop 0
	v_cvt_pk_bf16_f32 v0, v4, v5
	v_cvt_pk_bf16_f32 v1, v6, v7
	v_cvt_pk_bf16_f32 v2, v8, v9
	v_cvt_pk_bf16_f32 v3, v10, v11
	global_store_dwordx4 v[12:13], v[0:3], off offset:48
	s_cbranch_vccz .LBB7_449
	s_waitcnt lgkmcnt(0)
	s_barrier
	v_mov_b32_e32 v158, v79
	v_mov_b32_e32 v159, v78
	v_mov_b32_e32 v160, v77
	v_mov_b32_e32 v161, v76
	v_mov_b32_e32 v162, v75
	v_mov_b32_e32 v163, v74
	v_mov_b32_e32 v164, v73
	v_mov_b32_e32 v165, v72
	v_mov_b32_e32 v166, v71
	v_mov_b32_e32 v167, v70
	v_mov_b32_e32 v168, v69
	v_mov_b32_e32 v169, v68
	v_mov_b32_e32 v170, v67
	v_mov_b32_e32 v171, v66
	v_mov_b32_e32 v172, v65
	v_mov_b32_e32 v157, v64
	s_cbranch_execz .LBB7_450
